# DSA key-list building: per-lane 64-bit lowest-bit loop without branches or SALU in the body (lanes drop out through v_cmpx, wave exits on EXEC empty); lanes with more than 24 keys expanded wave-wide (
# speedup vs baseline: 1.0120x; 1.0120x over previous
.LBB0_700:
	v_add_u32_e32 v0, s46, v55
	s_waitcnt lgkmcnt(0)
	ds_read_b64 v[4:5], v0
	s_waitcnt lgkmcnt(0)
	v_bcnt_u32_b32 v0, v4, 0
	v_bcnt_u32_b32 v0, v5, v0
	v_mov_b64_e32 v[204:205], v[4:5]
	v_mov_b32_e32 v18, v0
	s_nop 1
	v_add_u32_dpp v18, v18, v18 row_shr:1 row_mask:0xf bank_mask:0xf
	s_nop 1
	v_add_u32_dpp v18, v18, v18 row_shr:2 row_mask:0xf bank_mask:0xf
	s_nop 1
	v_add_u32_dpp v18, v18, v18 row_shr:4 row_mask:0xf bank_mask:0xf
	s_nop 1
	v_add_u32_dpp v18, v18, v18 row_shr:8 row_mask:0xf bank_mask:0xf
	s_nop 1
	v_add_u32_dpp v18, v18, v18 row_bcast:15 row_mask:0xa bank_mask:0xf
	s_nop 1
	v_add_u32_dpp v18, v18, v18 row_bcast:31 row_mask:0xc bank_mask:0xf
	v_sub_u32_e32 v206, v18, v0
	v_cmp_lt_u32_e32 vcc, 24, v0
	s_mov_b64 s[100:101], vcc
	v_cndmask_b32_e32 v0, v0, v1, vcc
	v_sub_u32_e32 v13, s87, v206
	v_min_i32_e32 v0, v0, v13
	v_readlane_b32 s28, v18, 63
	v_lshl_add_u32 v12, v206, 1, s40
.Llist_w_a:
	v_cmpx_lt_i32_e32 vcc, 0, v0
	v_ffbl_b32_e32 v13, v4
	v_ffbl_b32_e32 v14, v5
	v_or_b32_e32 v14, 32, v14
	v_min_u32_e32 v13, v13, v14
	v_or_b32_e32 v13, v13, v8
	ds_write_b16 v12, v13
	v_add_co_u32_e32 v15, vcc, -1, v4
	v_addc_co_u32_e32 v16, vcc, -1, v5, vcc
	v_and_b32_e32 v4, v4, v15
	v_and_b32_e32 v5, v5, v16
	v_add_u32_e32 v12, 2, v12
	v_add_u32_e32 v0, -1, v0
	s_cbranch_execnz .Llist_w_a
	s_mov_b64 exec, -1
	s_mov_b64 s[12:13], s[100:101]
	s_cmp_eq_u64 s[12:13], 0
	s_cbranch_scc1 .Llist_dx_a
